# P5 gather_issue: per-thread staging row/column offsets precomputed once per phase instead of per unit
# speedup vs baseline: 1.0078x; 1.0078x over previous
; #define PG8_LAS __attribute__((address_space(3)))
; #define PG8_STAGE(bufoff, base, uoff, voff) do { _Pragma("unroll") for (int _i = 0; _i < 2; ++_i) \
;         __builtin_amdgcn_raw_ptr_buffer_load_lds((base), (PG8_LAS void*)(lds + (bufoff) + ldsw + _i * 8192), 16, (int)(voff)[_i], (int)(uoff), 0, 0); } while (0)
; #define PG8_WAIT_V(n) asm volatile("s_waitcnt vmcnt(" #n ")" ::: "memory")
; #define PG8_BAR __builtin_amdgcn_s_barrier()
; template <class Epi, class Sched, bool GATHER, int MODE>
; __device__ __forceinline__ void gemm_phase(PG8_LAS unsigned char* lds, PG8_LAS unsigned* scr, const Gemm g, const Sched& S, const Epi& E, int tid_in) {
;     ...
;         for (int i = 0; i < 2; ++i) { int R, C; stage_rc(tz * 16 + i * 8192, R, C);
; #pragma unroll
;             for (int h = 0; h < 2; ++h) __builtin_amdgcn_raw_ptr_buffer_load_lds(rs, (PG8_LAS void*)((PG8_LAS unsigned char*)(scr + 1024) + (2 * h + i) * 2048 + wid * 256), 4, (int)((unsigned)(uu.rb * 256 + h * 128 + R) * 4u), (int)so, 0, 0); } };
;     ...
;     if (GATHER) { gather_issue(cur); asm volatile("s_waitcnt vmcnt(0)" ::: "memory");
;         const u32x4 o = gather_read(cur); c0[0] = o[0]; c0[1] = o[1]; c1[0] = o[2]; c1[1] = o[3]; }
;     else { c0[0] = voffA[0]; c0[1] = voffA[1]; c1[0] = voffA[0]; c1[1] = voffA[1]; }
;     unsigned cA = GATHER ? 0u : (unsigned)cur.pm * tstep, cB = (unsigned)cur.pn * tstep;
;     PG8_STAGE(PG8_SB(0, 0), baseB, cB, voffB); PG8_STAGE(PG8_SB(0, 1), baseB, cB + hstep, voffB); PG8_STAGE(PG8_SA(0, 0), baseA, cA, c0); PG8_STAGE(PG8_SA(0, 1), baseA, cA + hstepA, c1);
;     if (wr == 1) PG8_BAR;
;     PG8_WAIT_V(2); PG8_BAR;
;     PG8_STAGE(PG8_SB(1, 0), baseB, cB + kstep, voffB); PG8_STAGE(PG8_SA(1, 0), baseA, cA + kstep, c0); PG8_STAGE(PG8_SB(1, 1), baseB, cB + hstep + kstep, voffB);
;     PG8_WAIT_V(6); PG8_BAR;
.LBB0_784:
	v_readlane_b32 s22, v255, 8
	s_lshl_b32 s92, s22, 16
	s_add_u32 s60, s27, 0x29400000
	s_addc_u32 s61, s29, 0
	s_lshl_b64 s[22:23], s[92:93], 2
	s_add_u32 s75, s10, s22
	s_addc_u32 s76, s11, s23
	s_add_u32 s77, s27, 0x6e400000
	s_addc_u32 s78, s29, 0
	s_add_u32 s79, s27, s22
	s_addc_u32 s80, s29, s23
	s_add_i32 s81, s67, 0x18000
	s_or_b32 s10, s41, 0x80
	s_mov_b32 s50, s6
	s_mov_b32 s51, s7
	s_mov_b32 m0, s81
	s_add_i32 s82, s67, 0x1a000
	s_waitcnt vmcnt(2)
	s_barrier
	buffer_load_dwordx4 v165, s[48:51], s10 offen lds
	s_mov_b32 m0, s82
	s_add_i32 s83, s67, 0x8000
	buffer_load_dwordx4 v180, s[48:51], s10 offen lds
	s_mov_b32 m0, s83
	s_movk_i32 s11, 0x80
	s_add_i32 s84, s67, 0xa000
	buffer_load_dwordx4 v185, s[4:7], s11 offen lds
	s_mov_b32 m0, s84
	s_add_i32 s85, s67, 0x1c000
	buffer_load_dwordx4 v202, s[4:7], s11 offen lds
	s_or_b32 s10, s41, 0x20080
	s_mov_b32 m0, s85
	s_add_i32 s86, s67, 0x1e000
	buffer_load_dwordx4 v165, s[48:51], s10 offen lds
	s_mov_b32 m0, s86
	v_and_b32_e32 v0, 15, v168
	buffer_load_dwordx4 v180, s[48:51], s10 offen lds
	v_and_b32_e32 v1, 48, v168
	v_lshlrev_b32_e32 v0, 6, v0
	v_lshlrev_b32_e32 v3, 2, v168
	v_or_b32_e32 v2, v0, v1
	s_lshl_b32 s10, s15, 13
	v_and_b32_e32 v4, 32, v3
	v_bitop3_b32 v0, v0, v4, v1 bitop3:0x36
	v_bitop3_b32 v1, v2, s10, v4 bitop3:0xde
	s_lshl_b32 s10, s13, 12
	s_and_b32 s10, s10, 0x3000
	s_waitcnt vmcnt(6)
	s_add_i32 s87, s67, 0xc000
	v_or_b32_e32 v0, s10, v0
	s_movk_i32 s55, 0x100
	s_movk_i32 s10, 0xff
	v_add_u32_e32 v2, 0x380, v168
	v_cmp_gt_i32_e32 vcc, s11, v168
	s_cmpk_lt_u32 s12, 0x100
	v_cmp_gt_i32_e64 s[34:35], s55, v168
	v_cmp_lt_i32_e64 s[36:37], s10, v168
	v_mov_b32_e32 v166, v168
	v_cndmask_b32_e32 v181, v2, v168, vcc
	s_cselect_b64 s[62:63], -1, 0
	v_add_u32_e32 v182, s42, v3
	s_add_i32 s88, s67, 0xe000
	s_add_i32 s89, s94, -1
	s_mov_b32 s38, 0
	v_add_u32_e32 v183, 0, v0
	v_add_u32_e32 v184, 0, v1
	s_barrier
	v_ashrrev_i32_e32 v236, 31, v168
	v_lshrrev_b32_e32 v236, 26, v236
	v_lshlrev_b32_e32 v237, 4, v168
	v_add_u32_e32 v236, v168, v236
	v_bfe_i32 v238, v168, 27, 1
	v_lshrrev_b32_e32 v238, 22, v238
	v_add_u32_e32 v238, v237, v238
	v_and_b32_e32 v238, 0xfffffc00, v238
	v_sub_u32_e32 v238, v237, v238
	v_lshrrev_b32_e32 v239, 4, v238
	v_ashrrev_i32_e32 v240, 31, v238
	v_ashrrev_i32_e32 v236, 6, v236
	v_and_b32_e32 v239, 32, v239
	v_lshrrev_b32_e32 v240, 26, v240
	v_lshlrev_b32_e32 v236, 3, v236
	v_xad_u32 v238, v239, v238, v240
	v_and_b32_e32 v236, 0x3ffffff0, v236
	v_ashrrev_i32_e32 v238, 6, v238
	v_add_lshl_u32 v250, v238, v236, 2
	v_add_u32_e32 v238, 0x2000, v237
	v_ashrrev_i32_e32 v237, 31, v238
	v_lshrrev_b32_e32 v237, 22, v237
	v_add_u32_e32 v237, v238, v237
	v_ashrrev_i32_e32 v237, 10, v237
	v_mul_i32_i24_e32 v236, 0x400, v237
	v_sub_u32_e32 v238, v238, v236
	v_lshrrev_b32_e32 v236, 4, v238
	v_ashrrev_i32_e32 v239, 31, v238
	v_and_b32_e32 v236, 32, v236
	v_lshrrev_b32_e32 v239, 26, v239
	v_lshlrev_b32_e32 v237, 3, v237
	v_xad_u32 v238, v236, v238, v239
	v_and_b32_e32 v237, 0x3ffffff0, v237
	v_ashrrev_i32_e32 v238, 6, v238
	v_add_lshl_u32 v251, v238, v237, 2
	s_branch .LBB0_787

; #define PG8_LAS __attribute__((address_space(3)))
;     __device__ __forceinline__ const int* gsrc() const { return (const int*)slot_dst; }
;     __device__ __forceinline__ unsigned gsoff(const Unit& u) const { return (unsigned)u.e * (unsigned)cap * 4u; }
; template <class Epi, class Sched, bool GATHER, int MODE>
; __device__ __forceinline__ void gemm_phase(PG8_LAS unsigned char* lds, PG8_LAS unsigned* scr, const Gemm g, const Sched& S, const Epi& E, int tid_in) {
;     ...
;     auto gather_issue = [&](const Unit& uu) { int tz = tid; asm volatile("" : "+v"(tz));
;         const __amdgpu_buffer_rsrc_t rs = __builtin_amdgcn_make_buffer_rsrc((void*)S.gsrc(), 0, (int)0xFFFFFFFFu, 0x00020000); const unsigned so = S.gsoff(uu);
; #pragma unroll
;         for (int i = 0; i < 2; ++i) { int R, C; stage_rc(tz * 16 + i * 8192, R, C);
; #pragma unroll
;             for (int h = 0; h < 2; ++h) __builtin_amdgcn_raw_ptr_buffer_load_lds(rs, (PG8_LAS void*)((PG8_LAS unsigned char*)(scr + 1024) + (2 * h + i) * 2048 + wid * 256), 4, (int)((unsigned)(uu.rb * 256 + h * 128 + R) * 4u), (int)so, 0, 0); } };
.LBB0_793:
	s_andn2_b64 vcc, exec, s[10:11]
	s_cbranch_vccnz .LBB0_795
	s_lshl_b32 s13, s30, 10
	s_mov_b32 m0, s31
	s_lshl_b32 s12, s14, 18
	v_add_u32_e32 v2, s13, v250
	s_mov_b32 s54, s6
	s_mov_b32 s55, s7
	s_or_b32 s22, s13, 0x200
	buffer_load_dword v2, s[52:55], s12 offen lds
	v_add_u32_e32 v0, s22, v250
	s_mov_b32 m0, s64
	s_nop 0
	buffer_load_dword v0, s[52:55], s12 offen lds
	v_add_u32_e32 v1, s13, v251
	s_mov_b32 m0, s65
	v_add_u32_e32 v0, s22, v251
	buffer_load_dword v1, s[52:55], s12 offen lds
	s_mov_b32 m0, s66
	s_nop 0
	buffer_load_dword v0, s[52:55], s12 offen lds
	s_movk_i32 s55, 0x100
